# speedup vs baseline: 1.0216x; 1.0163x over previous
_Z16sum_layer_kernelPKfS0_Pf:
	s_load_dwordx4 s[4:7], s[0:1], 0x0
	s_load_dwordx2 s[8:9], s[0:1], 0x10
	v_lshrrev_b32_e32 v42, 6, v0
	v_bfe_u32 v41, v0, 5, 1
	v_and_b32_e32 v40, 31, v0
	v_readfirstlane_b32 s23, v42
	v_and_b32_e32 v43, 7, v0
	v_bfe_u32 v44, v0, 3, 3
	s_lshl_b32 s3, s2, 12
	s_lshl_b32 s19, s2, 7
	s_lshl_b32 s23, s23, 12
	v_lshlrev_b32_e32 v1, 11, v41
	v_lshl_or_b32 v1, v40, 2, v1
	s_mov_b32 m0, s23
	v_lshrrev_b32_e32 v46, 1, v44
	v_xor_b32_e32 v46, v43, v46
	v_lshlrev_b32_e32 v46, 4, v46
	v_lshl_add_u32 v35, v44, 16, v46
	v_lshl_add_u32 v35, v42, 21, v35
	v_add_u32_e32 v35, s19, v35
	v_xor_b32_e32 v86, 64, v35
	s_mov_b32 s20, 0x7fc00
	s_mov_b32 s21, 0xff800
	s_mov_b32 s22, 0x17f400
	s_mov_b32 s14, 0x200000
	s_mov_b32 s15, 0x20000
	v_and_b32_e32 v45, 63, v0
	v_lshlrev_b32_e32 v37, 4, v45
	s_add_u32 s54, s23, 0x4000
	s_waitcnt lgkmcnt(0)
	s_mov_b32 s12, s6
	s_and_b32 s13, s7, 0xffff
	s_and_b32 s5, s5, 0xffff
	s_mov_b32 s6, 0x800000
	s_mov_b32 s7, s15
	s_mov_b32 m0, s54
	s_nop 0
	buffer_load_dwordx4 v37, s[12:15], s3 offen nt lds
	buffer_load_dwordx4 v37, s[12:15], s3 offen offset:1024 nt lds
	buffer_load_dwordx4 v37, s[12:15], s3 offen offset:2048 nt lds
	buffer_load_dwordx4 v37, s[12:15], s3 offen offset:3072 nt lds
	s_mov_b32 m0, s23
	s_nop 0
	buffer_load_dwordx4 v35, s[4:7], 0 offen nt lds
	buffer_load_dwordx4 v86, s[4:7], s20 offen offset:1024 nt lds
	buffer_load_dwordx4 v35, s[4:7], s21 offen offset:2048 nt lds
	buffer_load_dwordx4 v86, s[4:7], s22 offen offset:3072 nt lds
	v_and_b32_e32 v45, 63, v0
	v_lshlrev_b32_e32 v36, 2, v40
	v_lshl_add_u32 v36, v41, 18, v36
	v_lshl_add_u32 v36, v42, 21, v36
	v_add_u32_e32 v36, s19, v36
	v_bfe_u32 v47, v40, 1, 3
	v_lshlrev_b32_e32 v39, 2, v41
	v_xor_b32_e32 v39, v39, v47
	v_lshlrev_b32_e32 v39, 4, v39
	v_lshl_add_u32 v39, v40, 7, v39
	v_lshl_add_u32 v39, v42, 12, v39
	v_xor_b32_e32 v81, 16, v39
	v_xor_b32_e32 v82, 32, v39
	v_xor_b32_e32 v83, 48, v39
	v_cmp_gt_u32_e32 vcc, 32, v45
	v_mov_b32_e32 v34, 0xc1600000
	v_mov_b32_e32 v84, 0x3fb8aa3b
	v_mov_b32_e32 v85, 0x3f317218
	s_lshl_b32 s24, 1, 16
	s_lshl_b32 s25, 2, 16
	s_lshl_b32 s26, 3, 16
	s_lshl_b32 s27, 8, 16
	s_lshl_b32 s28, 9, 16
	s_lshl_b32 s29, 10, 16
	s_lshl_b32 s30, 11, 16
	s_lshl_b32 s31, 16, 16
	s_lshl_b32 s32, 17, 16
	s_lshl_b32 s33, 18, 16
	s_lshl_b32 s34, 19, 16
	s_lshl_b32 s35, 24, 16
	s_lshl_b32 s36, 25, 16
	s_lshl_b32 s37, 26, 16
	s_lshl_b32 s38, 27, 16
	s_and_b32 s9, s9, 0xffff
	s_mov_b32 s10, s6
	s_mov_b32 s11, s15
	v_lshl_add_u32 v38, v42, 12, v1
	v_add_u32_e32 v38, 0x4000, v38
	v_add_u32_e32 v87, 0x400, v38
	s_waitcnt vmcnt(4)
	ds_read2_b32 v[18:19], v38 offset0:0 offset1:32
	ds_read2_b32 v[20:21], v38 offset0:64 offset1:96
	ds_read2_b32 v[22:23], v38 offset0:128 offset1:160
	ds_read2_b32 v[24:25], v38 offset0:192 offset1:224
	ds_read2_b32 v[26:27], v87 offset0:0 offset1:32
	ds_read2_b32 v[28:29], v87 offset0:64 offset1:96
	ds_read2_b32 v[30:31], v87 offset0:128 offset1:160
	ds_read2_b32 v[32:33], v87 offset0:192 offset1:224
	s_waitcnt lgkmcnt(0)
	v_max3_f32 v48, v18, v19, v20
	v_max3_f32 v50, v21, v22, v23
	v_max3_f32 v48, v48, v24, v25
	v_max3_f32 v50, v50, v26, v27
	v_max3_f32 v48, v48, v28, v29
	v_max3_f32 v50, v50, v30, v31
	v_max3_f32 v48, v48, v32, v33
	v_max_f32_e32 v48, v48, v50
	v_mov_b32_e32 v50, v48
	s_nop 1
	v_permlane32_swap_b32_e32 v48, v50
	v_max_f32_e32 v48, v48, v50
	v_fmamk_f32 v48, v48, 0x3fb8aa3b, v34
	v_pk_fma_f32 v[18:19], v[18:19], v[84:85], v[48:49] op_sel_hi:[1,0,0] neg_lo:[0,0,1] neg_hi:[0,0,1]
	v_exp_f32_e32 v18, v18
	v_exp_f32_e32 v19, v19
	v_pk_fma_f32 v[20:21], v[20:21], v[84:85], v[48:49] op_sel_hi:[1,0,0] neg_lo:[0,0,1] neg_hi:[0,0,1]
	v_exp_f32_e32 v20, v20
	v_exp_f32_e32 v21, v21
	v_pk_fma_f32 v[22:23], v[22:23], v[84:85], v[48:49] op_sel_hi:[1,0,0] neg_lo:[0,0,1] neg_hi:[0,0,1]
	v_exp_f32_e32 v22, v22
	v_exp_f32_e32 v23, v23
	v_pk_fma_f32 v[24:25], v[24:25], v[84:85], v[48:49] op_sel_hi:[1,0,0] neg_lo:[0,0,1] neg_hi:[0,0,1]
	v_exp_f32_e32 v24, v24
	v_exp_f32_e32 v25, v25
	v_pk_fma_f32 v[26:27], v[26:27], v[84:85], v[48:49] op_sel_hi:[1,0,0] neg_lo:[0,0,1] neg_hi:[0,0,1]
	v_exp_f32_e32 v26, v26
	v_exp_f32_e32 v27, v27
	v_pk_fma_f32 v[28:29], v[28:29], v[84:85], v[48:49] op_sel_hi:[1,0,0] neg_lo:[0,0,1] neg_hi:[0,0,1]
	v_exp_f32_e32 v28, v28
	v_exp_f32_e32 v29, v29
	v_pk_fma_f32 v[30:31], v[30:31], v[84:85], v[48:49] op_sel_hi:[1,0,0] neg_lo:[0,0,1] neg_hi:[0,0,1]
	v_exp_f32_e32 v30, v30
	v_exp_f32_e32 v31, v31
	v_pk_fma_f32 v[32:33], v[32:33], v[84:85], v[48:49] op_sel_hi:[1,0,0] neg_lo:[0,0,1] neg_hi:[0,0,1]
	v_exp_f32_e32 v32, v32
	v_exp_f32_e32 v33, v33
	v_pk_add_f32 v[56:57], v[18:19], v[20:21]
	v_pk_add_f32 v[58:59], v[22:23], v[24:25]
	v_pk_add_f32 v[60:61], v[26:27], v[28:29]
	v_pk_add_f32 v[62:63], v[30:31], v[32:33]
	v_pk_add_f32 v[56:57], v[56:57], v[58:59]
	v_pk_add_f32 v[60:61], v[60:61], v[62:63]
	v_pk_add_f32 v[56:57], v[56:57], v[60:61]
	v_add_f32_e32 v50, v56, v57
	v_mov_b32_e32 v51, v50
	s_nop 1
	v_permlane32_swap_b32_e32 v50, v51
	v_add_f32_e32 v50, v50, v51
	v_log_f32_e32 v50, v50
	v_cvt_pk_f16_f32 v40, v18, v19
	v_cvt_pk_f16_f32 v41, v20, v21
	v_cvt_pk_f16_f32 v42, v22, v23
	v_cvt_pk_f16_f32 v43, v24, v25
	v_cvt_pk_f16_f32 v44, v26, v27
	v_cvt_pk_f16_f32 v45, v28, v29
	v_cvt_pk_f16_f32 v46, v30, v31
	v_cvt_pk_f16_f32 v47, v32, v33
	v_add_f32_e32 v50, 0x41600000, v50
	v_mul_f32_e32 v50, 0xbf317218, v50
	v_cndmask_b32_e64 v51, v50, 1.0, vcc
	s_waitcnt vmcnt(0)
	ds_read_b128 v[2:5], v39
	ds_read_b128 v[6:9], v81
	ds_read_b128 v[10:13], v82
	ds_read_b128 v[14:17], v83
	s_waitcnt lgkmcnt(2)
	v_max3_f32 v52, v2, v3, v4
	v_max3_f32 v53, v5, v6, v7
	v_max_f32_e32 v52, v52, v8
	v_max_f32_e32 v53, v53, v9
	s_waitcnt lgkmcnt(0)
	v_max3_f32 v52, v52, v10, v11
	v_max3_f32 v53, v53, v12, v13
	v_max3_f32 v52, v52, v14, v15
	v_max3_f32 v53, v53, v16, v17
	v_max_f32_e32 v52, v52, v53
	v_mov_b32_e32 v53, v52
	s_nop 1
	v_permlane32_swap_b32_e32 v52, v53
	v_max_f32_e32 v52, v52, v53
	v_cndmask_b32_e32 v54, 1.0, v52, vcc
	v_fmamk_f32 v48, v52, 0x3fb8aa3b, v34
	v_pk_fma_f32 v[2:3], v[2:3], v[84:85], v[48:49] op_sel_hi:[1,0,0] neg_lo:[0,0,1] neg_hi:[0,0,1]
	v_mfma_f32_32x32x2_f32 v[64:79], v54, v51, 0
	v_exp_f32_e32 v2, v2
	v_exp_f32_e32 v3, v3
	v_pk_fma_f32 v[4:5], v[4:5], v[84:85], v[48:49] op_sel_hi:[1,0,0] neg_lo:[0,0,1] neg_hi:[0,0,1]
	v_exp_f32_e32 v4, v4
	v_exp_f32_e32 v5, v5
	v_pk_fma_f32 v[6:7], v[6:7], v[84:85], v[48:49] op_sel_hi:[1,0,0] neg_lo:[0,0,1] neg_hi:[0,0,1]
	v_exp_f32_e32 v6, v6
	v_exp_f32_e32 v7, v7
	v_pk_fma_f32 v[8:9], v[8:9], v[84:85], v[48:49] op_sel_hi:[1,0,0] neg_lo:[0,0,1] neg_hi:[0,0,1]
	v_exp_f32_e32 v8, v8
	v_exp_f32_e32 v9, v9
	v_pk_fma_f32 v[10:11], v[10:11], v[84:85], v[48:49] op_sel_hi:[1,0,0] neg_lo:[0,0,1] neg_hi:[0,0,1]
	v_exp_f32_e32 v10, v10
	v_cvt_pk_f16_f32 v56, v2, v3
	v_cvt_pk_f16_f32 v57, v4, v5
	v_cvt_pk_f16_f32 v58, v6, v7
	v_cvt_pk_f16_f32 v59, v8, v9
	v_exp_f32_e32 v11, v11
	v_pk_fma_f32 v[12:13], v[12:13], v[84:85], v[48:49] op_sel_hi:[1,0,0] neg_lo:[0,0,1] neg_hi:[0,0,1]
	v_exp_f32_e32 v12, v12
	v_mfma_f32_32x32x16_f16 v[18:33], v[56:59], v[40:43], 0
	v_exp_f32_e32 v13, v13
	v_pk_fma_f32 v[14:15], v[14:15], v[84:85], v[48:49] op_sel_hi:[1,0,0] neg_lo:[0,0,1] neg_hi:[0,0,1]
	v_exp_f32_e32 v14, v14
	v_exp_f32_e32 v15, v15
	v_pk_fma_f32 v[16:17], v[16:17], v[84:85], v[48:49] op_sel_hi:[1,0,0] neg_lo:[0,0,1] neg_hi:[0,0,1]
	v_exp_f32_e32 v16, v16
	v_exp_f32_e32 v17, v17
	v_cvt_pk_f16_f32 v60, v10, v11
	v_cvt_pk_f16_f32 v61, v12, v13
	v_cvt_pk_f16_f32 v62, v14, v15
	v_cvt_pk_f16_f32 v63, v16, v17
	s_nop 1
	v_mfma_f32_32x32x16_f16 v[18:33], v[60:63], v[44:47], v[18:33]
	s_nop 11
	v_log_f32_e32 v18, v18
	v_log_f32_e32 v19, v19
	v_log_f32_e32 v20, v20
	v_log_f32_e32 v21, v21
	v_log_f32_e32 v22, v22
	v_log_f32_e32 v23, v23
	v_pk_fma_f32 v[64:65], v[18:19], v[84:85], v[64:65] op_sel:[0,1,0] op_sel_hi:[1,1,1]
	buffer_store_dword v64, v36, s[8:11], 0 offen sc0
	buffer_store_dword v65, v36, s[8:11], s24 offen sc0
	v_log_f32_e32 v24, v24
	v_log_f32_e32 v25, v25
	v_pk_fma_f32 v[66:67], v[20:21], v[84:85], v[66:67] op_sel:[0,1,0] op_sel_hi:[1,1,1]
	buffer_store_dword v66, v36, s[8:11], s25 offen sc0
	buffer_store_dword v67, v36, s[8:11], s26 offen sc0
	v_log_f32_e32 v26, v26
	v_log_f32_e32 v27, v27
	v_pk_fma_f32 v[68:69], v[22:23], v[84:85], v[68:69] op_sel:[0,1,0] op_sel_hi:[1,1,1]
	buffer_store_dword v68, v36, s[8:11], s27 offen sc0
	buffer_store_dword v69, v36, s[8:11], s28 offen sc0
	v_log_f32_e32 v28, v28
	v_log_f32_e32 v29, v29
	v_pk_fma_f32 v[70:71], v[24:25], v[84:85], v[70:71] op_sel:[0,1,0] op_sel_hi:[1,1,1]
	buffer_store_dword v70, v36, s[8:11], s29 offen sc0
	buffer_store_dword v71, v36, s[8:11], s30 offen sc0
	v_log_f32_e32 v30, v30
	v_log_f32_e32 v31, v31
	v_pk_fma_f32 v[72:73], v[26:27], v[84:85], v[72:73] op_sel:[0,1,0] op_sel_hi:[1,1,1]
	buffer_store_dword v72, v36, s[8:11], s31 offen sc0
	buffer_store_dword v73, v36, s[8:11], s32 offen sc0
	v_log_f32_e32 v32, v32
	v_log_f32_e32 v33, v33
	v_pk_fma_f32 v[74:75], v[28:29], v[84:85], v[74:75] op_sel:[0,1,0] op_sel_hi:[1,1,1]
	buffer_store_dword v74, v36, s[8:11], s33 offen sc0
	buffer_store_dword v75, v36, s[8:11], s34 offen sc0
	v_pk_fma_f32 v[76:77], v[30:31], v[84:85], v[76:77] op_sel:[0,1,0] op_sel_hi:[1,1,1]
	buffer_store_dword v76, v36, s[8:11], s35 offen sc0
	buffer_store_dword v77, v36, s[8:11], s36 offen sc0
	v_pk_fma_f32 v[78:79], v[32:33], v[84:85], v[78:79] op_sel:[0,1,0] op_sel_hi:[1,1,1]
	buffer_store_dword v78, v36, s[8:11], s37 offen sc0
	buffer_store_dword v79, v36, s[8:11], s38 offen sc0
	s_endpgm
